# MoE unit-list build (M1 and M2): the expert search reads the tile-prefix table once (8 ds_read_b128) and counts with arithmetic, instead of 16 dependent LDS round trips
# baseline (speedup 1.0000x reference)
; #define LAS __attribute__((address_space(3)))
;     DI void build(volatile LAS int* ulw, int tid) const {
;         if (tid < 32) { const int L = tid * G + c; const int xcd = L & 7, q = L >> 3; const int sr = (q >> 5) * 8 + xcd, slot = q & 31;
;             int mt = sr * GM + (slot % GM), nt_ = slot / GM; const int Mt = tb[32];
;             bool ok = mt < Mt; int half = 0;
;             const int rl = (Mt + 8 * GM - 1) / (8 * GM) - 1, m0 = rl * 8 * GM, Vm = Mt - m0, V = Vm * nN;
;             if (tid == rl && 2 * V <= G) { ok = c < 2 * V; const int v = c >> 1; mt = m0 + (ok ? v % Vm : 0); nt_ = ok ? v / Vm : 0; half = 1 + (c & 1); }
;             int e = 0; for (int k = 1; k < 32; ++k) e += (tb[k] <= mt) ? 1 : 0;
;             ulw[tid * 8 + 0] = ok ? mt : -1; ulw[tid * 8 + 1] = e; ulw[tid * 8 + 2] = mt - tb[e]; ulw[tid * 8 + 3] = cnt[e]; ulw[tid * 8 + 4] = nt_; ulw[tid * 8 + 5] = half; }
;     }
.LBB0_1185:
	s_or_b64 exec, exec, s[10:11]
	v_lshl_add_u32 v0, v0, 5, 0
	v_add_u32_e32 v0, 0x20300, v0
	v_mov_b32_e32 v100, 0x20040
	ds_read_b128 v[104:107], v100
	ds_read_b128 v[108:111], v100 offset:16
	ds_read_b128 v[112:115], v100 offset:32
	ds_read_b128 v[116:119], v100 offset:48
	ds_read_b128 v[120:123], v100 offset:64
	ds_read_b128 v[124:127], v100 offset:80
	ds_read_b128 v[128:131], v100 offset:96
	ds_read_b128 v[132:135], v100 offset:112
	v_mov_b32_e32 v5, 31
	s_waitcnt lgkmcnt(0)
	v_sub_u32_e32 v6, v3, v105
	v_ashrrev_i32_e32 v6, 31, v6
	v_add_u32_e32 v5, v5, v6
	v_sub_u32_e32 v6, v3, v106
	v_ashrrev_i32_e32 v6, 31, v6
	v_add_u32_e32 v5, v5, v6
	v_sub_u32_e32 v6, v3, v107
	v_ashrrev_i32_e32 v6, 31, v6
	v_add_u32_e32 v5, v5, v6
	v_sub_u32_e32 v6, v3, v108
	v_ashrrev_i32_e32 v6, 31, v6
	v_add_u32_e32 v5, v5, v6
	v_sub_u32_e32 v6, v3, v109
	v_ashrrev_i32_e32 v6, 31, v6
	v_add_u32_e32 v5, v5, v6
	v_sub_u32_e32 v6, v3, v110
	v_ashrrev_i32_e32 v6, 31, v6
	v_add_u32_e32 v5, v5, v6
	v_sub_u32_e32 v6, v3, v111
	v_ashrrev_i32_e32 v6, 31, v6
	v_add_u32_e32 v5, v5, v6
	v_sub_u32_e32 v6, v3, v112
	v_ashrrev_i32_e32 v6, 31, v6
	v_add_u32_e32 v5, v5, v6
	v_sub_u32_e32 v6, v3, v113
	v_ashrrev_i32_e32 v6, 31, v6
	v_add_u32_e32 v5, v5, v6
	v_sub_u32_e32 v6, v3, v114
	v_ashrrev_i32_e32 v6, 31, v6
	v_add_u32_e32 v5, v5, v6
	v_sub_u32_e32 v6, v3, v115
	v_ashrrev_i32_e32 v6, 31, v6
	v_add_u32_e32 v5, v5, v6
	v_sub_u32_e32 v6, v3, v116
	v_ashrrev_i32_e32 v6, 31, v6
	v_add_u32_e32 v5, v5, v6
	v_sub_u32_e32 v6, v3, v117
	v_ashrrev_i32_e32 v6, 31, v6
	v_add_u32_e32 v5, v5, v6
	v_sub_u32_e32 v6, v3, v118
	v_ashrrev_i32_e32 v6, 31, v6
	v_add_u32_e32 v5, v5, v6
	v_sub_u32_e32 v6, v3, v119
	v_ashrrev_i32_e32 v6, 31, v6
	v_add_u32_e32 v5, v5, v6
	v_sub_u32_e32 v6, v3, v120
	v_ashrrev_i32_e32 v6, 31, v6
	v_add_u32_e32 v5, v5, v6
	v_sub_u32_e32 v6, v3, v121
	v_ashrrev_i32_e32 v6, 31, v6
	v_add_u32_e32 v5, v5, v6
	v_sub_u32_e32 v6, v3, v122
	v_ashrrev_i32_e32 v6, 31, v6
	v_add_u32_e32 v5, v5, v6
	v_sub_u32_e32 v6, v3, v123
	v_ashrrev_i32_e32 v6, 31, v6
	v_add_u32_e32 v5, v5, v6
	v_sub_u32_e32 v6, v3, v124
	v_ashrrev_i32_e32 v6, 31, v6
	v_add_u32_e32 v5, v5, v6
	v_sub_u32_e32 v6, v3, v125
	v_ashrrev_i32_e32 v6, 31, v6
	v_add_u32_e32 v5, v5, v6
	v_sub_u32_e32 v6, v3, v126
	v_ashrrev_i32_e32 v6, 31, v6
	v_add_u32_e32 v5, v5, v6
	v_sub_u32_e32 v6, v3, v127
	v_ashrrev_i32_e32 v6, 31, v6
	v_add_u32_e32 v5, v5, v6
	v_sub_u32_e32 v6, v3, v128
	v_ashrrev_i32_e32 v6, 31, v6
	v_add_u32_e32 v5, v5, v6
	v_sub_u32_e32 v6, v3, v129
	v_ashrrev_i32_e32 v6, 31, v6
	v_add_u32_e32 v5, v5, v6
	v_sub_u32_e32 v6, v3, v130
	v_ashrrev_i32_e32 v6, 31, v6
	v_add_u32_e32 v5, v5, v6
	v_sub_u32_e32 v6, v3, v131
	v_ashrrev_i32_e32 v6, 31, v6
	v_add_u32_e32 v5, v5, v6
	v_sub_u32_e32 v6, v3, v132
	v_ashrrev_i32_e32 v6, 31, v6
	v_add_u32_e32 v5, v5, v6
	v_sub_u32_e32 v6, v3, v133
	v_ashrrev_i32_e32 v6, 31, v6
	v_add_u32_e32 v5, v5, v6
	v_sub_u32_e32 v6, v3, v134
	v_ashrrev_i32_e32 v6, 31, v6
	v_add_u32_e32 v5, v5, v6
	v_sub_u32_e32 v6, v3, v135
	v_ashrrev_i32_e32 v6, 31, v6
	v_add_u32_e32 v5, v5, v6
	v_cndmask_b32_e64 v6, -1, v3, s[8:9]
	ds_write_b32 v0, v6
	ds_write_b32 v0, v5 offset:4
	v_lshl_add_u32 v5, v5, 2, 0
	v_add_u32_e32 v6, 0x20040, v5
	ds_read_b32 v6, v6
	s_waitcnt lgkmcnt(0)
	v_sub_u32_e32 v3, v3, v6
	ds_write_b32 v0, v3 offset:8
	v_add_u32_e32 v3, 0x20200, v5
	ds_read_b32 v3, v3
	s_waitcnt lgkmcnt(0)
	ds_write_b32 v0, v3 offset:12
	ds_write_b32 v0, v2 offset:16
	ds_write_b32 v0, v4 offset:20
